# phase I: the per-token drains (now serving only the index loads) moved behind each token's finish so the next tokens' rows stay in flight
# baseline (speedup 1.0000x reference)
.LBB0_1229:
	s_add_i32 s29, s29, s12
	s_add_u32 s61, s61, s18
	s_addc_u32 s65, s65, s19
	s_add_u32 s62, s62, s20
	s_addc_u32 s63, s63, s21
	s_add_u32 s33, s33, s22
	s_addc_u32 s3, s3, s23
	s_add_i32 s4, s39, s29
	s_waitcnt vmcnt(0)
	v_mov_b64_e32 v[10:11], v[14:15]
	s_waitcnt vmcnt(0)
	v_mov_b64_e32 v[6:7], v[26:27]
	s_cmp_lt_i32 s4, 0x8000
	v_mov_b64_e32 v[12:13], v[16:17]
	v_mov_b64_e32 v[8:9], v[28:29]
	s_cbranch_scc0 .LBB0_1280
.LBB0_1230:
	s_waitcnt vmcnt(0)
	v_lshlrev_b32_e32 v14, 2, v22
	v_add_u32_e32 v14, s38, v14
	ds_read_b32 v14, v14
	v_lshlrev_b32_e32 v15, 2, v23
	v_lshlrev_b32_e32 v16, 2, v24
	v_add_u32_e32 v15, s38, v15
	v_add_u32_e32 v17, s38, v16
	v_lshlrev_b32_e32 v16, 2, v25
	v_add_u32_e32 v23, s38, v16
	ds_read_b32 v16, v15
	ds_read_b32 v22, v17
	ds_read_b32 v24, v23
	s_waitcnt lgkmcnt(3)
	v_ashrrev_i32_e32 v15, 31, v14
	v_mov_b32_e32 v214, v18
	v_lshlrev_b64 v[14:15], 18, v[14:15]
	s_waitcnt lgkmcnt(2)
	v_ashrrev_i32_e32 v17, 31, v16
	v_lshlrev_b64 v[26:27], 10, v[214:215]
	v_lshl_add_u64 v[14:15], s[10:11], 0, v[14:15]
	v_mov_b32_e32 v214, v19
	v_lshlrev_b64 v[16:17], 18, v[16:17]
	v_lshl_add_u64 v[14:15], v[14:15], 0, v[26:27]
	v_lshlrev_b64 v[18:19], 10, v[214:215]
	v_lshl_add_u64 v[16:17], s[10:11], 0, v[16:17]
	v_lshl_add_u64 v[14:15], v[14:15], 0, v[30:31]
	v_lshl_add_u64 v[16:17], v[16:17], 0, v[18:19]
	s_waitcnt lgkmcnt(1)
	v_ashrrev_i32_e32 v23, 31, v22
	v_lshl_add_u64 v[16:17], v[16:17], 0, v[30:31]
	global_load_dword v155, v[14:15], off
	global_load_dword v154, v[14:15], off offset:256
	global_load_dword v153, v[14:15], off offset:512
	global_load_dword v152, v[14:15], off offset:768
	global_load_dword v151, v[16:17], off
	global_load_dword v150, v[16:17], off offset:256
	global_load_dword v149, v[16:17], off offset:512
	global_load_dword v148, v[16:17], off offset:768
	v_mov_b32_e32 v214, v20
	v_lshlrev_b64 v[14:15], 18, v[22:23]
	v_lshlrev_b64 v[16:17], 10, v[214:215]
	v_lshl_add_u64 v[14:15], s[10:11], 0, v[14:15]
	s_waitcnt lgkmcnt(0)
	v_ashrrev_i32_e32 v25, 31, v24
	v_lshl_add_u64 v[14:15], v[14:15], 0, v[16:17]
	v_mov_b32_e32 v214, v21
	v_lshlrev_b64 v[16:17], 18, v[24:25]
	v_lshlrev_b64 v[18:19], 10, v[214:215]
	v_lshl_add_u64 v[16:17], s[10:11], 0, v[16:17]
	v_lshlrev_b32_e32 v28, 16, v88
	v_and_b32_e32 v29, 0xffff0000, v88
	v_lshlrev_b32_e32 v26, 16, v89
	v_and_b32_e32 v27, 0xffff0000, v89
	v_lshlrev_b32_e32 v88, 16, v84
	v_and_b32_e32 v89, 0xffff0000, v84
	v_lshl_add_u64 v[16:17], v[16:17], 0, v[18:19]
	v_lshlrev_b32_e32 v20, 16, v92
	v_and_b32_e32 v21, 0xffff0000, v92
	v_lshlrev_b32_e32 v18, 16, v93
	v_and_b32_e32 v19, 0xffff0000, v93
	v_lshlrev_b32_e32 v24, 16, v90
	v_and_b32_e32 v25, 0xffff0000, v90
	v_lshlrev_b32_e32 v22, 16, v91
	v_and_b32_e32 v23, 0xffff0000, v91
	v_lshlrev_b32_e32 v84, 16, v85
	v_and_b32_e32 v85, 0xffff0000, v85
	v_sub_f32_e32 v89, v89, v86
	v_sub_f32_e32 v88, v88, v86
	v_sub_f32_e32 v19, v19, v86
	v_sub_f32_e32 v18, v18, v86
	v_sub_f32_e32 v21, v21, v86
	v_sub_f32_e32 v20, v20, v86
	v_sub_f32_e32 v23, v23, v86
	v_sub_f32_e32 v22, v22, v86
	v_sub_f32_e32 v25, v25, v86
	v_sub_f32_e32 v24, v24, v86
	v_sub_f32_e32 v27, v27, v86
	v_sub_f32_e32 v26, v26, v86
	v_sub_f32_e32 v29, v29, v86
	v_sub_f32_e32 v28, v28, v86
	v_sub_f32_e32 v85, v85, v86
	v_sub_f32_e32 v84, v84, v86
	v_pk_mul_f32 v[88:89], v[86:87], v[88:89] op_sel:[1,0]
	v_pk_mul_f32 v[20:21], v[86:87], v[20:21] op_sel:[1,0]
	v_pk_mul_f32 v[18:19], v[86:87], v[18:19] op_sel:[1,0]
	v_pk_mul_f32 v[24:25], v[86:87], v[24:25] op_sel:[1,0]
	v_pk_mul_f32 v[22:23], v[86:87], v[22:23] op_sel:[1,0]
	v_pk_mul_f32 v[28:29], v[86:87], v[28:29] op_sel:[1,0]
	v_pk_mul_f32 v[26:27], v[86:87], v[26:27] op_sel:[1,0]
	v_pk_mul_f32 v[84:85], v[86:87], v[84:85] op_sel:[1,0]
	v_pk_fma_f32 v[86:87], v[58:59], v[88:89], v[62:63]
	v_cvt_pk_f32_fp8_e32 v[88:89], v139
	v_cvt_pk_f32_fp8_sdwa v[90:91], v139 src0_sel:WORD_1
	v_cvt_pk_f32_fp8_e32 v[92:93], v138
	v_cvt_pk_f32_fp8_sdwa v[94:95], v138 src0_sel:WORD_1
	v_pk_mul_f32 v[2:3], v[2:3], s[72:73] op_sel_hi:[1,0]
	v_pk_fma_f32 v[18:19], v[32:33], v[18:19], v[36:37]
	v_pk_fma_f32 v[20:21], v[34:35], v[20:21], v[38:39]
	v_pk_fma_f32 v[22:23], v[40:41], v[22:23], v[44:45]
	v_pk_fma_f32 v[24:25], v[42:43], v[24:25], v[46:47]
	v_pk_fma_f32 v[20:21], v[2:3], v[88:89], v[20:21] op_sel_hi:[0,1,1]
	v_pk_fma_f32 v[18:19], v[2:3], v[90:91], v[18:19] op_sel_hi:[0,1,1]
	v_pk_fma_f32 v[24:25], v[2:3], v[92:93], v[24:25] op_sel_hi:[0,1,1]
	v_pk_fma_f32 v[22:23], v[2:3], v[94:95], v[22:23] op_sel_hi:[0,1,1]
	v_cvt_pk_f32_fp8_e32 v[88:89], v137
	v_cvt_pk_f32_fp8_sdwa v[90:91], v137 src0_sel:WORD_1
	v_cvt_pk_f32_fp8_e32 v[92:93], v136
	v_cvt_pk_f32_fp8_sdwa v[94:95], v136 src0_sel:WORD_1
	v_pk_fma_f32 v[26:27], v[48:49], v[26:27], v[52:53]
	v_pk_fma_f32 v[28:29], v[50:51], v[28:29], v[54:55]
	v_pk_fma_f32 v[84:85], v[56:57], v[84:85], v[60:61]
	v_pk_fma_f32 v[28:29], v[2:3], v[88:89], v[28:29] op_sel_hi:[0,1,1]
	v_pk_fma_f32 v[26:27], v[2:3], v[90:91], v[26:27] op_sel_hi:[0,1,1]
	v_pk_fma_f32 v[86:87], v[2:3], v[92:93], v[86:87] op_sel_hi:[0,1,1]
	v_pk_fma_f32 v[84:85], v[2:3], v[94:95], v[84:85] op_sel_hi:[0,1,1]
	v_cvt_pk_f32_fp8_sdwa v[88:89], v143 src0_sel:WORD_1
	v_cvt_pk_f32_fp8_e32 v[90:91], v143
	v_cvt_pk_f32_fp8_sdwa v[92:93], v142 src0_sel:WORD_1
	v_cvt_pk_f32_fp8_e32 v[94:95], v142
	v_pk_fma_f32 v[18:19], v[2:3], v[88:89], v[18:19] op_sel:[1,0,0]
	v_pk_fma_f32 v[20:21], v[2:3], v[90:91], v[20:21] op_sel:[1,0,0]
	v_pk_fma_f32 v[22:23], v[2:3], v[92:93], v[22:23] op_sel:[1,0,0]
	v_pk_fma_f32 v[24:25], v[2:3], v[94:95], v[24:25] op_sel:[1,0,0]
	v_cvt_pk_f32_fp8_sdwa v[88:89], v141 src0_sel:WORD_1
	v_cvt_pk_f32_fp8_e32 v[90:91], v141
	v_cvt_pk_f32_fp8_sdwa v[92:93], v140 src0_sel:WORD_1
	v_cvt_pk_f32_fp8_e32 v[94:95], v140
	v_pk_fma_f32 v[26:27], v[2:3], v[88:89], v[26:27] op_sel:[1,0,0]
	v_pk_fma_f32 v[28:29], v[2:3], v[90:91], v[28:29] op_sel:[1,0,0]
	v_pk_fma_f32 v[84:85], v[2:3], v[92:93], v[84:85] op_sel:[1,0,0]
	v_pk_fma_f32 v[2:3], v[2:3], v[94:95], v[86:87] op_sel:[1,0,0]
	v_cvt_pk_f32_fp8_e32 v[86:87], v147
	v_cvt_pk_f32_fp8_sdwa v[88:89], v147 src0_sel:WORD_1
	v_cvt_pk_f32_fp8_e32 v[90:91], v146
	v_cvt_pk_f32_fp8_sdwa v[92:93], v146 src0_sel:WORD_1
	v_pk_mul_f32 v[4:5], v[4:5], s[72:73] op_sel_hi:[1,0]
	v_cvt_pk_f32_fp8_sdwa v[94:95], v132 src0_sel:WORD_1
	v_pk_fma_f32 v[20:21], v[4:5], v[86:87], v[20:21] op_sel_hi:[0,1,1]
	v_pk_fma_f32 v[18:19], v[4:5], v[88:89], v[18:19] op_sel_hi:[0,1,1]
	v_pk_fma_f32 v[86:87], v[4:5], v[90:91], v[24:25] op_sel_hi:[0,1,1]
	v_pk_fma_f32 v[88:89], v[4:5], v[92:93], v[22:23] op_sel_hi:[0,1,1]
	v_cvt_pk_f32_fp8_e32 v[22:23], v145
	v_cvt_pk_f32_fp8_sdwa v[24:25], v145 src0_sel:WORD_1
	v_cvt_pk_f32_fp8_e32 v[90:91], v144
	v_cvt_pk_f32_fp8_sdwa v[92:93], v144 src0_sel:WORD_1
	v_pk_fma_f32 v[28:29], v[4:5], v[22:23], v[28:29] op_sel_hi:[0,1,1]
	v_pk_fma_f32 v[26:27], v[4:5], v[24:25], v[26:27] op_sel_hi:[0,1,1]
	v_cvt_pk_f32_fp8_sdwa v[22:23], v135 src0_sel:WORD_1
	v_cvt_pk_f32_fp8_e32 v[24:25], v135
	v_pk_fma_f32 v[2:3], v[4:5], v[90:91], v[2:3] op_sel_hi:[0,1,1]
	v_pk_fma_f32 v[92:93], v[4:5], v[92:93], v[84:85] op_sel_hi:[0,1,1]
	v_cvt_pk_f32_fp8_sdwa v[84:85], v134 src0_sel:WORD_1
	v_cvt_pk_f32_fp8_e32 v[90:91], v134
	v_pk_fma_f32 v[22:23], v[4:5], v[22:23], v[18:19] op_sel:[1,0,0]
	v_pk_fma_f32 v[24:25], v[4:5], v[24:25], v[20:21] op_sel:[1,0,0]
	v_cvt_pk_f32_fp8_sdwa v[18:19], v133 src0_sel:WORD_1
	v_cvt_pk_f32_fp8_e32 v[20:21], v133
	v_cvt_pk_f32_fp8_e32 v[96:97], v132
	v_pk_fma_f32 v[88:89], v[4:5], v[84:85], v[88:89] op_sel:[1,0,0]
	v_pk_fma_f32 v[90:91], v[4:5], v[90:91], v[86:87] op_sel:[1,0,0]
	v_pk_fma_f32 v[84:85], v[4:5], v[18:19], v[26:27] op_sel:[1,0,0]
	v_pk_fma_f32 v[86:87], v[4:5], v[20:21], v[28:29] op_sel:[1,0,0]
	v_pk_fma_f32 v[26:27], v[4:5], v[94:95], v[92:93] op_sel:[1,0,0]
	v_pk_fma_f32 v[28:29], v[4:5], v[96:97], v[2:3] op_sel:[1,0,0]
	v_pk_mov_b32 v[2:3], v[24:25], v[22:23] op_sel:[1,0]
	v_mov_b32_e32 v4, v24
	v_mov_b32_e32 v5, v23
	v_pk_add_f32 v[2:3], v[2:3], v[4:5]
	v_pk_mov_b32 v[4:5], v[90:91], v[88:89] op_sel:[1,0]
	v_mov_b32_e32 v18, v90
	v_mov_b32_e32 v19, v89
	v_pk_add_f32 v[4:5], v[4:5], v[18:19]
	v_add_f32_e32 v2, v2, v3
	v_pk_add_f32 v[4:5], v[4:5], v[4:5] op_sel:[0,1] op_sel_hi:[1,0]
	v_add_f32_e32 v2, 0, v2
	v_add_f32_e32 v18, v86, v87
	v_add_f32_e32 v20, v84, v85
	v_mov_b32_e32 v3, v28
	v_mov_b32_e32 v5, v29
	v_mov_b32_e32 v19, v26
	v_mov_b32_e32 v21, v27
	v_pk_add_f32 v[2:3], v[2:3], v[4:5]
	v_pk_add_f32 v[4:5], v[18:19], v[20:21]
	s_add_i32 s24, s59, s29
	v_pk_add_f32 v[2:3], v[2:3], v[4:5]
	s_min_i32 s4, s24, 0x7fff
	v_add_f32_e32 v2, v2, v3
	ds_bpermute_b32 v3, v126, v2
	s_ashr_i32 s5, s4, 31
	s_lshl_b64 s[6:7], s[4:5], 3
	s_add_u32 s6, s45, s6
	s_addc_u32 s7, s54, s7
	s_waitcnt lgkmcnt(0)
	v_add_f32_e32 v4, v2, v3
	ds_bpermute_b32 v5, v127, v4
	s_lshl_b64 s[4:5], s[4:5], 11
	v_lshl_add_u64 v[14:15], v[14:15], 0, v[30:31]
	v_lshl_add_u64 v[2:3], v[78:79], 0, s[4:5]
	v_lshl_add_u64 v[16:17], v[16:17], 0, v[30:31]
	s_waitcnt lgkmcnt(0)
	v_add_f32_e32 v4, v4, v5
	ds_bpermute_b32 v5, v128, v4
	global_load_dword v163, v[14:15], off
	global_load_dword v162, v[14:15], off offset:256
	global_load_dword v161, v[14:15], off offset:512
	global_load_dword v160, v[14:15], off offset:768
	global_load_dword v159, v[16:17], off
	global_load_dword v158, v[16:17], off offset:256
	global_load_dword v157, v[16:17], off offset:512
	global_load_dword v156, v[16:17], off offset:768
	global_load_dwordx2 v[102:103], v[2:3], off
	global_load_dwordx2 v[100:101], v[2:3], off offset:512
	global_load_dwordx2 v[98:99], v[2:3], off offset:1024
	global_load_dwordx2 v[94:95], v[2:3], off offset:1536
	s_add_i32 s4, s13, s29
	s_min_i32 s26, s4, 0x7fff
	s_waitcnt lgkmcnt(0)
	v_add_f32_e32 v2, v4, v5
	ds_bpermute_b32 v3, v129, v2
	s_lshl_b32 s4, s26, 2
	s_ashr_i32 s5, s4, 31
	s_lshl_b64 s[76:77], s[4:5], 2
	s_add_u32 s4, s40, s76
	s_waitcnt lgkmcnt(0)
	v_add_f32_e32 v2, v2, v3
	ds_bpermute_b32 v3, v130, v2
	s_addc_u32 s5, s56, s77
	global_load_dwordx2 v[96:97], v215, s[6:7]
	global_load_dwordx4 v[14:17], v215, s[4:5]
	s_add_u32 s4, s80, s76
	s_addc_u32 s5, s81, s77
	s_waitcnt lgkmcnt(0)
	v_add_f32_e32 v2, v2, v3
	ds_bpermute_b32 v3, v131, v2
	s_add_u32 s6, s57, s76
	s_addc_u32 s7, s75, s77
	s_waitcnt lgkmcnt(0)
	v_add_f32_e32 v92, v2, v3
	v_fmamk_f32 v25, v92, 0xba800000, v25
	v_fmac_f32_e32 v24, 0xba800000, v92
	v_fmamk_f32 v23, v92, 0xba800000, v23
	v_fmac_f32_e32 v22, 0xba800000, v92
	v_pk_mul_f32 v[2:3], v[22:23], v[22:23]
	v_pk_mul_f32 v[4:5], v[24:25], v[24:25]
	v_fmamk_f32 v89, v92, 0xba800000, v89
	v_pk_mov_b32 v[18:19], v[4:5], v[2:3] op_sel:[1,0]
	v_mov_b32_e32 v5, v3
	v_pk_add_f32 v[2:3], v[18:19], v[4:5]
	v_fmac_f32_e32 v88, 0xba800000, v92
	v_fmamk_f32 v91, v92, 0xba800000, v91
	v_fmac_f32_e32 v90, 0xba800000, v92
	v_pk_add_f32 v[2:3], v[2:3], v[2:3] op_sel_hi:[0,1]
	v_pk_mul_f32 v[4:5], v[88:89], v[88:89]
	v_pk_mul_f32 v[18:19], v[90:91], v[90:91]
	v_fmac_f32_e32 v86, 0xba800000, v92
	v_pk_mov_b32 v[20:21], v[18:19], v[4:5] op_sel:[1,0]
	v_mov_b32_e32 v19, v5
	v_fmac_f32_e32 v84, 0xba800000, v92
	v_fmamk_f32 v87, v92, 0xba800000, v87
	v_mul_f32_e32 v2, v86, v86
	v_pk_add_f32 v[4:5], v[20:21], v[18:19]
	v_fmamk_f32 v85, v92, 0xba800000, v85
	v_pk_fma_f32 v[18:19], v[86:87], v[86:87], v[2:3] op_sel_hi:[1,1,0]
	v_mul_f32_e32 v2, v84, v84
	v_pk_add_f32 v[4:5], v[4:5], v[4:5] op_sel_hi:[0,1]
	v_pk_fma_f32 v[20:21], v[84:85], v[84:85], v[2:3] op_sel_hi:[1,1,0]
	v_fmamk_f32 v27, v92, 0xba800000, v27
	v_fmac_f32_e32 v26, 0xba800000, v92
	v_fmamk_f32 v29, v92, 0xba800000, v29
	v_fmac_f32_e32 v28, 0xba800000, v92
	v_mul_f32_e32 v18, v28, v28
	v_mul_f32_e32 v20, v29, v29
	v_mul_f32_e32 v2, v26, v26
	v_mul_f32_e32 v4, v27, v27
	v_pk_add_f32 v[18:19], v[18:19], v[20:21]
	v_pk_add_f32 v[2:3], v[2:3], v[4:5]
	s_nop 0
	v_pk_add_f32 v[2:3], v[18:19], v[2:3]
	s_nop 0
	v_add_f32_e32 v92, v2, v3
	global_load_dwordx4 v[18:21], v215, s[4:5]
	global_load_dwordx4 v[2:5], v215, s[6:7]
	ds_bpermute_b32 v93, v126, v92
	s_waitcnt lgkmcnt(0)
	v_add_f32_e32 v92, v92, v93
	ds_bpermute_b32 v93, v127, v92
	s_waitcnt lgkmcnt(0)
	v_add_f32_e32 v92, v92, v93
	ds_bpermute_b32 v93, v128, v92
	s_waitcnt lgkmcnt(0)
	v_add_f32_e32 v92, v92, v93
	ds_bpermute_b32 v93, v129, v92
	s_waitcnt lgkmcnt(0)
	v_add_f32_e32 v92, v92, v93
	ds_bpermute_b32 v93, v130, v92
	s_waitcnt lgkmcnt(0)
	v_add_f32_e32 v92, v92, v93
	ds_bpermute_b32 v93, v131, v92
	s_waitcnt lgkmcnt(0)
	v_add_f32_e32 v92, v92, v93
	v_fmamk_f32 v92, v92, 0x3a800000, v240
	v_mul_f32_e32 v93, 0x4f800000, v92
	v_cmp_gt_f32_e32 vcc, s36, v92
	s_nop 1
	v_cndmask_b32_e32 v92, v92, v93, vcc
	v_sqrt_f32_e32 v93, v92
	s_nop 0
	v_add_u32_e32 v104, -1, v93
	v_fma_f32 v105, -v104, v93, v92
	v_cmp_ge_f32_e64 s[4:5], 0, v105
	v_add_u32_e32 v105, 1, v93
	s_nop 0
	v_cndmask_b32_e64 v104, v93, v104, s[4:5]
	v_fma_f32 v93, -v105, v93, v92
	v_cmp_lt_f32_e64 s[4:5], 0, v93
	s_nop 1
	v_cndmask_b32_e64 v93, v104, v105, s[4:5]
	v_mul_f32_e32 v104, 0x37800000, v93
	v_cndmask_b32_e32 v93, v93, v104, vcc
	v_cmp_class_f32_e32 vcc, v92, v234
	s_and_b64 s[4:5], s[14:15], exec
	s_nop 0
	v_cndmask_b32_e32 v92, v93, v92, vcc
	v_div_scale_f32 v93, s[4:5], v92, v92, 1.0
	v_rcp_f32_e32 v104, v93
	s_cselect_b32 s5, s63, 0
	s_cselect_b32 s4, s62, 0
	s_cmp_lg_u64 s[4:5], 0
	v_fma_f32 v105, -v93, v104, 1.0
	v_fmac_f32_e32 v104, v105, v104
	v_div_scale_f32 v105, vcc, 1.0, v92, 1.0
	v_mul_f32_e32 v106, v105, v104
	v_fma_f32 v107, -v93, v106, v105
	v_fmac_f32_e32 v106, v107, v104
	v_fma_f32 v93, -v93, v106, v105
	v_div_fmas_f32 v93, v93, v104, v106
	v_div_fixup_f32 v106, v93, v92, 1.0
	v_pk_mul_f32 v[92:93], v[24:25], v[106:107] op_sel_hi:[1,0]
	v_pk_mul_f32 v[22:23], v[22:23], v[106:107] op_sel_hi:[1,0]
	s_cselect_b64 s[76:77], -1, 0
	s_cmp_eq_u64 s[4:5], 0
	v_lshl_add_u64 v[104:105], v[30:31], 2, s[4:5]
	v_pk_fma_f32 v[24:25], v[176:177], v[22:23], v[194:195]
	v_pk_fma_f32 v[22:23], v[174:175], v[92:93], v[192:193]
	s_cbranch_scc1 .LBB0_1232
	global_store_dwordx4 v[104:105], v[22:25], off

.LBB0_1234:
	s_nop 0
	v_mov_b32_e32 v136, v106
	v_mov_b32_e32 v137, v106
	v_mov_b32_e32 v107, v106
	v_pk_mul_f32 v[88:89], v[88:89], v[136:137]
	v_pk_mul_f32 v[90:91], v[90:91], v[106:107]
	s_andn2_b64 vcc, exec, s[76:77]
	v_pk_fma_f32 v[24:25], v[88:89], v[180:181], v[198:199]
	v_cndmask_b32_e64 v88, 0, 1, s[76:77]
	v_pk_fma_f32 v[22:23], v[90:91], v[178:179], v[196:197]
	v_cmp_ne_u32_e64 s[6:7], 1, v88
	s_cbranch_vccnz .LBB0_1236
	global_store_dwordx4 v[104:105], v[22:25], off offset:1024

.LBB0_1246:
	s_waitcnt vmcnt(0)
	v_lshlrev_b32_e32 v14, 2, v14
	v_add_u32_e32 v14, s38, v14
	ds_read_b32 v22, v14
	v_mov_b32_e32 v214, v18
	v_lshlrev_b64 v[24:25], 10, v[214:215]
	v_lshlrev_b32_e32 v14, 2, v15
	v_add_u32_e32 v14, s38, v14
	s_waitcnt lgkmcnt(0)
	v_ashrrev_i32_e32 v23, 31, v22
	v_lshlrev_b64 v[22:23], 18, v[22:23]
	v_lshl_add_u64 v[22:23], s[10:11], 0, v[22:23]
	v_lshl_add_u64 v[22:23], v[22:23], 0, v[24:25]
	v_lshl_add_u64 v[22:23], v[22:23], 0, v[30:31]
	global_load_dword v139, v[22:23], off
	global_load_dword v138, v[22:23], off offset:256
	global_load_dword v137, v[22:23], off offset:512
	global_load_dword v136, v[22:23], off offset:768
	ds_read_b32 v14, v14
	v_mov_b32_e32 v214, v19
	v_lshlrev_b64 v[18:19], 10, v[214:215]
	v_mov_b32_e32 v214, v20
	s_ashr_i32 s27, s26, 31
	s_waitcnt lgkmcnt(0)
	v_ashrrev_i32_e32 v15, 31, v14
	v_lshlrev_b64 v[14:15], 18, v[14:15]
	v_lshl_add_u64 v[14:15], s[10:11], 0, v[14:15]
	v_lshl_add_u64 v[14:15], v[14:15], 0, v[18:19]
	v_lshl_add_u64 v[14:15], v[14:15], 0, v[30:31]
	global_load_dword v143, v[14:15], off
	global_load_dword v142, v[14:15], off offset:256
	global_load_dword v141, v[14:15], off offset:512
	global_load_dword v140, v[14:15], off offset:768
	v_lshlrev_b32_e32 v14, 2, v16
	v_add_u32_e32 v14, s38, v14
	ds_read_b32 v14, v14
	v_lshlrev_b64 v[18:19], 10, v[214:215]
	v_mov_b32_e32 v214, v21
	s_lshl_b64 s[6:7], s[26:27], 3
	s_add_u32 s6, s45, s6
	s_waitcnt lgkmcnt(0)
	v_ashrrev_i32_e32 v15, 31, v14
	v_lshlrev_b64 v[14:15], 18, v[14:15]
	v_lshl_add_u64 v[14:15], s[10:11], 0, v[14:15]
	v_lshl_add_u64 v[14:15], v[14:15], 0, v[18:19]
	v_lshl_add_u64 v[14:15], v[14:15], 0, v[30:31]
	global_load_dword v147, v[14:15], off
	global_load_dword v146, v[14:15], off offset:256
	global_load_dword v145, v[14:15], off offset:512
	global_load_dword v144, v[14:15], off offset:768
	v_lshlrev_b32_e32 v14, 2, v17
	v_add_u32_e32 v14, s38, v14
	ds_read_b32 v14, v14
	v_lshlrev_b64 v[16:17], 10, v[214:215]
	s_addc_u32 s7, s54, s7
	s_waitcnt lgkmcnt(0)
	v_ashrrev_i32_e32 v15, 31, v14
	v_lshlrev_b64 v[14:15], 18, v[14:15]
	v_lshl_add_u64 v[14:15], s[10:11], 0, v[14:15]
	v_lshl_add_u64 v[14:15], v[14:15], 0, v[16:17]
	v_lshl_add_u64 v[14:15], v[14:15], 0, v[30:31]
	global_load_dword v135, v[14:15], off
	global_load_dword v134, v[14:15], off offset:256
	global_load_dword v133, v[14:15], off offset:512
	global_load_dword v132, v[14:15], off offset:768
	global_load_dwordx2 v[86:87], v215, s[6:7]
	s_lshl_b64 s[6:7], s[26:27], 11
	v_lshl_add_u64 v[14:15], v[78:79], 0, s[6:7]
	s_add_i32 s6, s60, s29
	s_min_i32 s26, s6, 0x7fff
	s_lshl_b32 s6, s26, 2
	s_ashr_i32 s7, s6, 31
	s_lshl_b64 s[6:7], s[6:7], 2
	s_add_u32 s76, s40, s6
	s_addc_u32 s77, s56, s7
	global_load_dwordx2 v[92:93], v[14:15], off
	global_load_dwordx2 v[90:91], v[14:15], off offset:512
	global_load_dwordx2 v[88:89], v[14:15], off offset:1024
	global_load_dwordx2 v[84:85], v[14:15], off offset:1536
	global_load_dwordx4 v[22:25], v215, s[76:77]
	s_add_u32 s76, s80, s6
	s_addc_u32 s77, s81, s7
	s_add_u32 s6, s57, s6
	s_addc_u32 s7, s75, s7
	global_load_dwordx4 v[18:21], v215, s[76:77]
	global_load_dwordx4 v[14:17], v215, s[6:7]
	s_add_i32 s76, s97, s29
	s_cmpk_gt_i32 s76, 0x7fff
	s_cbranch_scc1 .LBB0_1263
	v_lshlrev_b32_e32 v106, 16, v64
	v_and_b32_e32 v107, 0xffff0000, v64
	v_lshlrev_b32_e32 v28, 16, v76
	v_and_b32_e32 v29, 0xffff0000, v76
	v_lshlrev_b32_e32 v26, 16, v77
	v_and_b32_e32 v27, 0xffff0000, v77
	v_lshlrev_b32_e32 v76, 16, v74
	v_and_b32_e32 v77, 0xffff0000, v74
	v_lshlrev_b32_e32 v74, 16, v75
	v_and_b32_e32 v75, 0xffff0000, v75
	v_lshlrev_b32_e32 v104, 16, v72
	v_and_b32_e32 v105, 0xffff0000, v72
	v_lshlrev_b32_e32 v72, 16, v73
	v_and_b32_e32 v73, 0xffff0000, v73
	v_lshlrev_b32_e32 v64, 16, v65
	v_and_b32_e32 v65, 0xffff0000, v65
	v_sub_f32_e32 v107, v107, v70
	v_sub_f32_e32 v106, v106, v70
	v_sub_f32_e32 v27, v27, v70
	v_sub_f32_e32 v26, v26, v70
	v_sub_f32_e32 v29, v29, v70
	v_sub_f32_e32 v28, v28, v70
	v_sub_f32_e32 v75, v75, v70
	v_sub_f32_e32 v74, v74, v70
	v_sub_f32_e32 v77, v77, v70
	v_sub_f32_e32 v76, v76, v70
	v_sub_f32_e32 v73, v73, v70
	v_sub_f32_e32 v72, v72, v70
	v_sub_f32_e32 v105, v105, v70
	v_sub_f32_e32 v104, v104, v70
	v_sub_f32_e32 v65, v65, v70
	v_sub_f32_e32 v64, v64, v70
	v_pk_mul_f32 v[106:107], v[70:71], v[106:107] op_sel:[1,0]
	v_pk_mul_f32 v[28:29], v[70:71], v[28:29] op_sel:[1,0]
	v_pk_mul_f32 v[26:27], v[70:71], v[26:27] op_sel:[1,0]
	v_pk_mul_f32 v[76:77], v[70:71], v[76:77] op_sel:[1,0]
	v_pk_mul_f32 v[74:75], v[70:71], v[74:75] op_sel:[1,0]
	v_pk_mul_f32 v[104:105], v[70:71], v[104:105] op_sel:[1,0]
	v_pk_mul_f32 v[72:73], v[70:71], v[72:73] op_sel:[1,0]
	v_pk_mul_f32 v[64:65], v[70:71], v[64:65] op_sel:[1,0]
	v_pk_fma_f32 v[70:71], v[58:59], v[106:107], v[62:63]
	v_cvt_pk_f32_fp8_e32 v[106:107], v113
	v_cvt_pk_f32_fp8_sdwa v[108:109], v113 src0_sel:WORD_1
	v_cvt_pk_f32_fp8_e32 v[164:165], v112
	v_cvt_pk_f32_fp8_sdwa v[112:113], v112 src0_sel:WORD_1
	v_pk_mul_f32 v[10:11], v[10:11], s[72:73] op_sel_hi:[1,0]
	v_pk_fma_f32 v[26:27], v[32:33], v[26:27], v[36:37]
	v_pk_fma_f32 v[28:29], v[34:35], v[28:29], v[38:39]
	v_pk_fma_f32 v[74:75], v[40:41], v[74:75], v[44:45]
	v_pk_fma_f32 v[28:29], v[10:11], v[106:107], v[28:29] op_sel_hi:[0,1,1]
	v_pk_fma_f32 v[26:27], v[10:11], v[108:109], v[26:27] op_sel_hi:[0,1,1]
	v_pk_fma_f32 v[74:75], v[10:11], v[112:113], v[74:75] op_sel_hi:[0,1,1]
	v_cvt_pk_f32_fp8_e32 v[106:107], v111
	v_cvt_pk_f32_fp8_sdwa v[108:109], v111 src0_sel:WORD_1
	v_cvt_pk_f32_fp8_e32 v[112:113], v110
	v_cvt_pk_f32_fp8_sdwa v[110:111], v110 src0_sel:WORD_1
	v_pk_fma_f32 v[72:73], v[48:49], v[72:73], v[52:53]
	v_pk_fma_f32 v[104:105], v[50:51], v[104:105], v[54:55]
	v_pk_fma_f32 v[64:65], v[56:57], v[64:65], v[60:61]
	v_pk_fma_f32 v[104:105], v[10:11], v[106:107], v[104:105] op_sel_hi:[0,1,1]
	v_pk_fma_f32 v[72:73], v[10:11], v[108:109], v[72:73] op_sel_hi:[0,1,1]
	v_pk_fma_f32 v[70:71], v[10:11], v[112:113], v[70:71] op_sel_hi:[0,1,1]
	v_pk_fma_f32 v[64:65], v[10:11], v[110:111], v[64:65] op_sel_hi:[0,1,1]
	v_cvt_pk_f32_fp8_sdwa v[106:107], v117 src0_sel:WORD_1
	v_cvt_pk_f32_fp8_e32 v[108:109], v117
	v_cvt_pk_f32_fp8_sdwa v[110:111], v116 src0_sel:WORD_1
	v_cvt_pk_f32_fp8_e32 v[112:113], v116
	v_pk_fma_f32 v[76:77], v[42:43], v[76:77], v[46:47]
	v_pk_fma_f32 v[26:27], v[10:11], v[106:107], v[26:27] op_sel:[1,0,0]
	v_pk_fma_f32 v[76:77], v[10:11], v[164:165], v[76:77] op_sel_hi:[0,1,1]
	v_pk_fma_f32 v[28:29], v[10:11], v[108:109], v[28:29] op_sel:[1,0,0]
	v_pk_fma_f32 v[74:75], v[10:11], v[110:111], v[74:75] op_sel:[1,0,0]
	v_pk_fma_f32 v[76:77], v[10:11], v[112:113], v[76:77] op_sel:[1,0,0]
	v_cvt_pk_f32_fp8_sdwa v[106:107], v115 src0_sel:WORD_1
	v_cvt_pk_f32_fp8_e32 v[108:109], v115
	v_cvt_pk_f32_fp8_sdwa v[110:111], v114 src0_sel:WORD_1
	v_cvt_pk_f32_fp8_e32 v[112:113], v114
	v_pk_fma_f32 v[72:73], v[10:11], v[106:107], v[72:73] op_sel:[1,0,0]
	v_pk_fma_f32 v[104:105], v[10:11], v[108:109], v[104:105] op_sel:[1,0,0]
	v_pk_fma_f32 v[64:65], v[10:11], v[110:111], v[64:65] op_sel:[1,0,0]
	v_pk_fma_f32 v[10:11], v[10:11], v[112:113], v[70:71] op_sel:[1,0,0]
	v_cvt_pk_f32_fp8_e32 v[70:71], v121
	v_cvt_pk_f32_fp8_sdwa v[106:107], v121 src0_sel:WORD_1
	v_cvt_pk_f32_fp8_e32 v[108:109], v120
	v_cvt_pk_f32_fp8_sdwa v[110:111], v120 src0_sel:WORD_1
	v_pk_mul_f32 v[12:13], v[12:13], s[72:73] op_sel_hi:[1,0]
	s_ashr_i32 s77, s76, 31
	v_pk_fma_f32 v[28:29], v[12:13], v[70:71], v[28:29] op_sel_hi:[0,1,1]
	v_pk_fma_f32 v[26:27], v[12:13], v[106:107], v[26:27] op_sel_hi:[0,1,1]
	v_pk_fma_f32 v[70:71], v[12:13], v[108:109], v[76:77] op_sel_hi:[0,1,1]
	v_pk_fma_f32 v[74:75], v[12:13], v[110:111], v[74:75] op_sel_hi:[0,1,1]
	v_cvt_pk_f32_fp8_e32 v[76:77], v119
	v_cvt_pk_f32_fp8_sdwa v[106:107], v119 src0_sel:WORD_1
	v_cvt_pk_f32_fp8_e32 v[108:109], v118
	v_cvt_pk_f32_fp8_sdwa v[110:111], v118 src0_sel:WORD_1
	v_pk_fma_f32 v[76:77], v[12:13], v[76:77], v[104:105] op_sel_hi:[0,1,1]
	v_pk_fma_f32 v[104:105], v[12:13], v[106:107], v[72:73] op_sel_hi:[0,1,1]
	v_pk_fma_f32 v[10:11], v[12:13], v[108:109], v[10:11] op_sel_hi:[0,1,1]
	v_pk_fma_f32 v[106:107], v[12:13], v[110:111], v[64:65] op_sel_hi:[0,1,1]
	v_cvt_pk_f32_fp8_sdwa v[64:65], v125 src0_sel:WORD_1
	v_cvt_pk_f32_fp8_e32 v[72:73], v125
	v_cvt_pk_f32_fp8_sdwa v[108:109], v124 src0_sel:WORD_1
	v_cvt_pk_f32_fp8_e32 v[110:111], v124
	v_pk_fma_f32 v[112:113], v[12:13], v[64:65], v[26:27] op_sel:[1,0,0]
	v_pk_fma_f32 v[114:115], v[12:13], v[72:73], v[28:29] op_sel:[1,0,0]
	v_pk_fma_f32 v[72:73], v[12:13], v[108:109], v[74:75] op_sel:[1,0,0]
	v_pk_fma_f32 v[74:75], v[12:13], v[110:111], v[70:71] op_sel:[1,0,0]
	v_cvt_pk_f32_fp8_sdwa v[26:27], v123 src0_sel:WORD_1
	v_cvt_pk_f32_fp8_e32 v[28:29], v123
	v_cvt_pk_f32_fp8_sdwa v[108:109], v122 src0_sel:WORD_1
	v_cvt_pk_f32_fp8_e32 v[110:111], v122
	v_pk_fma_f32 v[64:65], v[12:13], v[26:27], v[104:105] op_sel:[1,0,0]
	v_pk_fma_f32 v[70:71], v[12:13], v[28:29], v[76:77] op_sel:[1,0,0]
	v_pk_fma_f32 v[26:27], v[12:13], v[108:109], v[106:107] op_sel:[1,0,0]
	v_pk_fma_f32 v[28:29], v[12:13], v[110:111], v[10:11] op_sel:[1,0,0]
	v_pk_mov_b32 v[10:11], v[114:115], v[112:113] op_sel:[1,0]
	v_mov_b32_e32 v12, v114
	v_mov_b32_e32 v13, v113
	v_pk_add_f32 v[10:11], v[10:11], v[12:13]
	v_pk_mov_b32 v[12:13], v[74:75], v[72:73] op_sel:[1,0]
	v_mov_b32_e32 v76, v74
	v_mov_b32_e32 v77, v73
	v_pk_add_f32 v[12:13], v[12:13], v[76:77]
	v_add_f32_e32 v10, v10, v11
	v_pk_add_f32 v[12:13], v[12:13], v[12:13] op_sel:[0,1] op_sel_hi:[1,0]
	v_add_f32_e32 v10, 0, v10
	v_add_f32_e32 v76, v70, v71
	v_add_f32_e32 v104, v64, v65
	v_mov_b32_e32 v11, v28
	v_mov_b32_e32 v13, v29
	v_mov_b32_e32 v77, v26
	v_mov_b32_e32 v105, v27
	v_pk_add_f32 v[10:11], v[10:11], v[12:13]
	v_pk_add_f32 v[12:13], v[76:77], v[104:105]
	s_lshl_b64 s[6:7], s[76:77], 12
	v_pk_add_f32 v[10:11], v[10:11], v[12:13]
	s_add_u32 s25, s8, s6
	v_add_f32_e32 v10, v10, v11
	ds_bpermute_b32 v11, v126, v10
	s_addc_u32 s27, s9, s7
	s_waitcnt lgkmcnt(0)
	v_add_f32_e32 v10, v10, v11
	ds_bpermute_b32 v11, v127, v10
	s_waitcnt lgkmcnt(0)
	v_add_f32_e32 v10, v10, v11
	ds_bpermute_b32 v11, v128, v10
	s_waitcnt lgkmcnt(0)
	v_add_f32_e32 v10, v10, v11
	ds_bpermute_b32 v11, v129, v10
	s_waitcnt lgkmcnt(0)
	v_add_f32_e32 v10, v10, v11
	ds_bpermute_b32 v11, v130, v10
	s_waitcnt lgkmcnt(0)
	v_add_f32_e32 v10, v10, v11
	ds_bpermute_b32 v11, v131, v10
	s_waitcnt lgkmcnt(0)
	v_add_f32_e32 v106, v10, v11
	v_fmamk_f32 v115, v106, 0xba800000, v115
	v_fmac_f32_e32 v114, 0xba800000, v106
	v_fmamk_f32 v113, v106, 0xba800000, v113
	v_fmac_f32_e32 v112, 0xba800000, v106
	v_pk_mul_f32 v[10:11], v[112:113], v[112:113]
	v_pk_mul_f32 v[12:13], v[114:115], v[114:115]
	v_fmamk_f32 v73, v106, 0xba800000, v73
	v_pk_mov_b32 v[76:77], v[12:13], v[10:11] op_sel:[1,0]
	v_mov_b32_e32 v13, v11
	v_pk_add_f32 v[10:11], v[76:77], v[12:13]
	v_fmac_f32_e32 v72, 0xba800000, v106
	v_fmamk_f32 v75, v106, 0xba800000, v75
	v_fmac_f32_e32 v74, 0xba800000, v106
	v_pk_add_f32 v[10:11], v[10:11], v[10:11] op_sel_hi:[0,1]
	v_pk_mul_f32 v[12:13], v[72:73], v[72:73]
	v_pk_mul_f32 v[76:77], v[74:75], v[74:75]
	v_fmac_f32_e32 v70, 0xba800000, v106
	v_pk_mov_b32 v[104:105], v[76:77], v[12:13] op_sel:[1,0]
	v_mov_b32_e32 v77, v13
	v_fmac_f32_e32 v64, 0xba800000, v106
	v_fmamk_f32 v71, v106, 0xba800000, v71
	v_mul_f32_e32 v10, v70, v70
	v_pk_add_f32 v[12:13], v[104:105], v[76:77]
	v_fmamk_f32 v65, v106, 0xba800000, v65
	v_pk_fma_f32 v[76:77], v[70:71], v[70:71], v[10:11] op_sel_hi:[1,1,0]
	v_mul_f32_e32 v10, v64, v64
	v_pk_add_f32 v[12:13], v[12:13], v[12:13] op_sel_hi:[0,1]
	v_pk_fma_f32 v[104:105], v[64:65], v[64:65], v[10:11] op_sel_hi:[1,1,0]
	v_fmamk_f32 v27, v106, 0xba800000, v27
	v_fmac_f32_e32 v26, 0xba800000, v106
	v_fmamk_f32 v29, v106, 0xba800000, v29
	v_fmac_f32_e32 v28, 0xba800000, v106
	v_mul_f32_e32 v76, v28, v28
	v_mul_f32_e32 v104, v29, v29
	v_mul_f32_e32 v10, v26, v26
	v_mul_f32_e32 v12, v27, v27
	v_pk_add_f32 v[76:77], v[76:77], v[104:105]
	v_pk_add_f32 v[10:11], v[10:11], v[12:13]
	s_nop 0
	v_pk_add_f32 v[10:11], v[76:77], v[10:11]
	s_nop 0
	v_add_f32_e32 v76, v10, v11
	ds_bpermute_b32 v77, v126, v76
	s_waitcnt lgkmcnt(0)
	v_add_f32_e32 v76, v76, v77
	ds_bpermute_b32 v77, v127, v76
	s_waitcnt lgkmcnt(0)
	v_add_f32_e32 v76, v76, v77
	ds_bpermute_b32 v77, v128, v76
	s_waitcnt lgkmcnt(0)
	v_add_f32_e32 v76, v76, v77
	ds_bpermute_b32 v77, v129, v76
	s_waitcnt lgkmcnt(0)
	v_add_f32_e32 v76, v76, v77
	ds_bpermute_b32 v77, v130, v76
	s_waitcnt lgkmcnt(0)
	v_add_f32_e32 v76, v76, v77
	ds_bpermute_b32 v77, v131, v76
	s_waitcnt lgkmcnt(0)
	v_add_f32_e32 v76, v76, v77
	v_fmamk_f32 v76, v76, 0x3a800000, v240
	v_mul_f32_e32 v77, 0x4f800000, v76
	v_cmp_gt_f32_e32 vcc, s36, v76
	s_nop 1
	v_cndmask_b32_e32 v76, v76, v77, vcc
	v_sqrt_f32_e32 v77, v76
	s_nop 0
	v_add_u32_e32 v104, -1, v77
	v_fma_f32 v105, -v104, v77, v76
	v_cmp_ge_f32_e64 s[6:7], 0, v105
	v_add_u32_e32 v105, 1, v77
	s_nop 0
	v_cndmask_b32_e64 v104, v77, v104, s[6:7]
	v_fma_f32 v77, -v105, v77, v76
	v_cmp_lt_f32_e64 s[6:7], 0, v77
	s_nop 1
	v_cndmask_b32_e64 v77, v104, v105, s[6:7]
	v_mul_f32_e32 v104, 0x37800000, v77
	v_cndmask_b32_e32 v77, v77, v104, vcc
	v_cmp_class_f32_e32 vcc, v76, v234
	s_and_b64 s[6:7], s[14:15], exec
	s_nop 0
	v_cndmask_b32_e32 v76, v77, v76, vcc
	v_div_scale_f32 v77, s[6:7], v76, v76, 1.0
	v_rcp_f32_e32 v104, v77
	s_cselect_b32 s7, s27, 0
	s_cselect_b32 s6, s25, 0
	s_cmp_lg_u64 s[6:7], 0
	v_fma_f32 v105, -v77, v104, 1.0
	v_fmac_f32_e32 v104, v105, v104
	v_div_scale_f32 v105, vcc, 1.0, v76, 1.0
	v_mul_f32_e32 v106, v105, v104
	v_fma_f32 v107, -v77, v106, v105
	v_fmac_f32_e32 v106, v107, v104
	v_fma_f32 v77, -v77, v106, v105
	v_div_fmas_f32 v77, v77, v104, v106
	v_div_fixup_f32 v106, v77, v76, 1.0
	v_pk_mul_f32 v[76:77], v[114:115], v[106:107] op_sel_hi:[1,0]
	v_pk_mul_f32 v[112:113], v[112:113], v[106:107] op_sel_hi:[1,0]
	s_cselect_b64 s[78:79], -1, 0
	s_cmp_eq_u64 s[6:7], 0
	v_lshl_add_u64 v[104:105], v[30:31], 2, s[6:7]
	v_pk_fma_f32 v[12:13], v[176:177], v[112:113], v[194:195]
	v_pk_fma_f32 v[10:11], v[174:175], v[76:77], v[192:193]
	s_cbranch_scc1 .LBB0_1249
	global_store_dwordx4 v[104:105], v[10:13], off

.LBB0_1263:
	s_waitcnt vmcnt(0)
	s_waitcnt vmcnt(2)
	v_lshlrev_b32_e32 v10, 2, v22
	v_add_u32_e32 v10, s38, v10
	ds_read_b32 v10, v10
	s_waitcnt vmcnt(1)
	v_mov_b32_e32 v214, v18
	v_lshlrev_b64 v[12:13], 10, v[214:215]
	v_mov_b32_e32 v214, v19
	s_ashr_i32 s27, s26, 31
	s_waitcnt lgkmcnt(0)
	v_ashrrev_i32_e32 v11, 31, v10
	v_lshlrev_b64 v[10:11], 18, v[10:11]
	v_lshl_add_u64 v[10:11], s[10:11], 0, v[10:11]
	v_lshl_add_u64 v[10:11], v[10:11], 0, v[12:13]
	v_lshl_add_u64 v[10:11], v[10:11], 0, v[30:31]
	global_load_dword v113, v[10:11], off
	global_load_dword v112, v[10:11], off offset:256
	global_load_dword v111, v[10:11], off offset:512
	global_load_dword v110, v[10:11], off offset:768
	v_lshlrev_b32_e32 v10, 2, v23
	v_add_u32_e32 v10, s38, v10
	ds_read_b32 v10, v10
	v_lshlrev_b64 v[12:13], 10, v[214:215]
	v_mov_b32_e32 v214, v20
	s_lshl_b64 s[6:7], s[26:27], 3
	s_add_u32 s6, s45, s6
	s_waitcnt lgkmcnt(0)
	v_ashrrev_i32_e32 v11, 31, v10
	v_lshlrev_b64 v[10:11], 18, v[10:11]
	v_lshl_add_u64 v[10:11], s[10:11], 0, v[10:11]
	v_lshl_add_u64 v[10:11], v[10:11], 0, v[12:13]
	v_lshl_add_u64 v[10:11], v[10:11], 0, v[30:31]
	global_load_dword v117, v[10:11], off
	global_load_dword v116, v[10:11], off offset:256
	global_load_dword v115, v[10:11], off offset:512
	global_load_dword v114, v[10:11], off offset:768
	v_lshlrev_b32_e32 v10, 2, v24
	v_add_u32_e32 v10, s38, v10
	ds_read_b32 v10, v10
	v_lshlrev_b64 v[12:13], 10, v[214:215]
	v_mov_b32_e32 v214, v21
	s_addc_u32 s7, s54, s7
	s_waitcnt lgkmcnt(0)
	v_ashrrev_i32_e32 v11, 31, v10
	v_lshlrev_b64 v[10:11], 18, v[10:11]
	v_lshl_add_u64 v[10:11], s[10:11], 0, v[10:11]
	v_lshl_add_u64 v[10:11], v[10:11], 0, v[12:13]
	v_lshl_add_u64 v[10:11], v[10:11], 0, v[30:31]
	global_load_dword v121, v[10:11], off
	global_load_dword v120, v[10:11], off offset:256
	global_load_dword v119, v[10:11], off offset:512
	global_load_dword v118, v[10:11], off offset:768
	v_lshlrev_b32_e32 v10, 2, v25
	v_add_u32_e32 v10, s38, v10
	ds_read_b32 v10, v10
	v_lshlrev_b64 v[12:13], 10, v[214:215]
	s_waitcnt lgkmcnt(0)
	v_ashrrev_i32_e32 v11, 31, v10
	v_lshlrev_b64 v[10:11], 18, v[10:11]
	v_lshl_add_u64 v[10:11], s[10:11], 0, v[10:11]
	v_lshl_add_u64 v[10:11], v[10:11], 0, v[12:13]
	v_lshl_add_u64 v[10:11], v[10:11], 0, v[30:31]
	global_load_dword v125, v[10:11], off
	global_load_dword v124, v[10:11], off offset:256
	global_load_dword v123, v[10:11], off offset:512
	global_load_dword v122, v[10:11], off offset:768
	global_load_dwordx2 v[70:71], v215, s[6:7]
	s_lshl_b64 s[6:7], s[26:27], 11
	v_lshl_add_u64 v[10:11], v[78:79], 0, s[6:7]
	s_add_i32 s6, s89, s29
	s_min_i32 s6, s6, 0x7fff
	s_lshl_b32 s6, s6, 2
	s_ashr_i32 s7, s6, 31
	s_lshl_b64 s[6:7], s[6:7], 2
	s_add_u32 s26, s40, s6
	s_addc_u32 s27, s56, s7
	global_load_dwordx2 v[76:77], v[10:11], off
	global_load_dwordx2 v[74:75], v[10:11], off offset:512
	global_load_dwordx2 v[72:73], v[10:11], off offset:1024
	global_load_dwordx2 v[64:65], v[10:11], off offset:1536
	global_load_dwordx4 v[22:25], v215, s[26:27]
	s_add_u32 s26, s80, s6
	s_addc_u32 s27, s81, s7
	s_add_u32 s6, s57, s6
	s_addc_u32 s7, s75, s7
	global_load_dwordx4 v[18:21], v215, s[26:27]
	global_load_dwordx4 v[26:29], v215, s[6:7]
	s_cmpk_gt_i32 s24, 0x7fff
	s_cbranch_scc1 .LBB0_1229
	v_lshlrev_b32_e32 v106, 16, v94
	v_and_b32_e32 v107, 0xffff0000, v94
	v_lshlrev_b32_e32 v12, 16, v102
	v_and_b32_e32 v13, 0xffff0000, v102
	v_lshlrev_b32_e32 v10, 16, v103
	v_and_b32_e32 v11, 0xffff0000, v103
	v_lshlrev_b32_e32 v102, 16, v100
	v_and_b32_e32 v103, 0xffff0000, v100
	v_lshlrev_b32_e32 v100, 16, v101
	v_and_b32_e32 v101, 0xffff0000, v101
	v_lshlrev_b32_e32 v104, 16, v98
	v_and_b32_e32 v105, 0xffff0000, v98
	v_lshlrev_b32_e32 v98, 16, v99
	v_and_b32_e32 v99, 0xffff0000, v99
	v_lshlrev_b32_e32 v94, 16, v95
	v_and_b32_e32 v95, 0xffff0000, v95
	v_sub_f32_e32 v107, v107, v96
	v_sub_f32_e32 v106, v106, v96
	v_sub_f32_e32 v11, v11, v96
	v_sub_f32_e32 v10, v10, v96
	v_sub_f32_e32 v13, v13, v96
	v_sub_f32_e32 v12, v12, v96
	v_sub_f32_e32 v101, v101, v96
	v_sub_f32_e32 v100, v100, v96
	v_sub_f32_e32 v103, v103, v96
	v_sub_f32_e32 v102, v102, v96
	v_sub_f32_e32 v99, v99, v96
	v_sub_f32_e32 v98, v98, v96
	v_sub_f32_e32 v105, v105, v96
	v_sub_f32_e32 v104, v104, v96
	v_sub_f32_e32 v95, v95, v96
	v_sub_f32_e32 v94, v94, v96
	v_pk_mul_f32 v[106:107], v[96:97], v[106:107] op_sel:[1,0]
	v_pk_mul_f32 v[12:13], v[96:97], v[12:13] op_sel:[1,0]
	v_pk_mul_f32 v[10:11], v[96:97], v[10:11] op_sel:[1,0]
	v_pk_mul_f32 v[102:103], v[96:97], v[102:103] op_sel:[1,0]
	v_pk_mul_f32 v[100:101], v[96:97], v[100:101] op_sel:[1,0]
	v_pk_mul_f32 v[104:105], v[96:97], v[104:105] op_sel:[1,0]
	v_pk_mul_f32 v[98:99], v[96:97], v[98:99] op_sel:[1,0]
	v_pk_mul_f32 v[94:95], v[96:97], v[94:95] op_sel:[1,0]
	v_pk_fma_f32 v[96:97], v[58:59], v[106:107], v[62:63]
	v_cvt_pk_f32_fp8_e32 v[106:107], v155
	v_cvt_pk_f32_fp8_sdwa v[108:109], v155 src0_sel:WORD_1
	v_cvt_pk_f32_fp8_e32 v[164:165], v154
	v_cvt_pk_f32_fp8_sdwa v[154:155], v154 src0_sel:WORD_1
	v_pk_mul_f32 v[6:7], v[6:7], s[72:73] op_sel_hi:[1,0]
	v_pk_fma_f32 v[10:11], v[32:33], v[10:11], v[36:37]
	v_pk_fma_f32 v[12:13], v[34:35], v[12:13], v[38:39]
	v_pk_fma_f32 v[100:101], v[40:41], v[100:101], v[44:45]
	v_pk_fma_f32 v[12:13], v[6:7], v[106:107], v[12:13] op_sel_hi:[0,1,1]
	v_pk_fma_f32 v[10:11], v[6:7], v[108:109], v[10:11] op_sel_hi:[0,1,1]
	v_pk_fma_f32 v[100:101], v[6:7], v[154:155], v[100:101] op_sel_hi:[0,1,1]
	v_cvt_pk_f32_fp8_e32 v[106:107], v153
	v_cvt_pk_f32_fp8_sdwa v[108:109], v153 src0_sel:WORD_1
	v_cvt_pk_f32_fp8_e32 v[154:155], v152
	v_cvt_pk_f32_fp8_sdwa v[152:153], v152 src0_sel:WORD_1
	v_pk_fma_f32 v[98:99], v[48:49], v[98:99], v[52:53]
	v_pk_fma_f32 v[104:105], v[50:51], v[104:105], v[54:55]
	v_pk_fma_f32 v[94:95], v[56:57], v[94:95], v[60:61]
	v_pk_fma_f32 v[104:105], v[6:7], v[106:107], v[104:105] op_sel_hi:[0,1,1]
	v_pk_fma_f32 v[98:99], v[6:7], v[108:109], v[98:99] op_sel_hi:[0,1,1]
	v_pk_fma_f32 v[94:95], v[6:7], v[152:153], v[94:95] op_sel_hi:[0,1,1]
	v_cvt_pk_f32_fp8_sdwa v[106:107], v151 src0_sel:WORD_1
	v_cvt_pk_f32_fp8_e32 v[108:109], v151
	v_cvt_pk_f32_fp8_sdwa v[152:153], v150 src0_sel:WORD_1
	v_cvt_pk_f32_fp8_e32 v[150:151], v150
	v_pk_fma_f32 v[102:103], v[42:43], v[102:103], v[46:47]
	v_pk_fma_f32 v[10:11], v[6:7], v[106:107], v[10:11] op_sel:[1,0,0]
	v_pk_fma_f32 v[102:103], v[6:7], v[164:165], v[102:103] op_sel_hi:[0,1,1]
	v_pk_fma_f32 v[12:13], v[6:7], v[108:109], v[12:13] op_sel:[1,0,0]
	v_pk_fma_f32 v[102:103], v[6:7], v[150:151], v[102:103] op_sel:[1,0,0]
	v_cvt_pk_f32_fp8_sdwa v[106:107], v149 src0_sel:WORD_1
	v_cvt_pk_f32_fp8_e32 v[108:109], v149
	v_cvt_pk_f32_fp8_sdwa v[150:151], v148 src0_sel:WORD_1
	v_cvt_pk_f32_fp8_e32 v[148:149], v148
	v_pk_fma_f32 v[96:97], v[6:7], v[154:155], v[96:97] op_sel_hi:[0,1,1]
	v_pk_fma_f32 v[100:101], v[6:7], v[152:153], v[100:101] op_sel:[1,0,0]
	v_pk_fma_f32 v[98:99], v[6:7], v[106:107], v[98:99] op_sel:[1,0,0]
	v_pk_fma_f32 v[104:105], v[6:7], v[108:109], v[104:105] op_sel:[1,0,0]
	v_pk_fma_f32 v[94:95], v[6:7], v[150:151], v[94:95] op_sel:[1,0,0]
	v_pk_fma_f32 v[6:7], v[6:7], v[148:149], v[96:97] op_sel:[1,0,0]
	v_cvt_pk_f32_fp8_e32 v[96:97], v163
	v_cvt_pk_f32_fp8_sdwa v[106:107], v163 src0_sel:WORD_1
	v_cvt_pk_f32_fp8_e32 v[108:109], v162
	v_cvt_pk_f32_fp8_sdwa v[148:149], v162 src0_sel:WORD_1
	v_pk_mul_f32 v[8:9], v[8:9], s[72:73] op_sel_hi:[1,0]
	s_ashr_i32 s25, s24, 31
	v_pk_fma_f32 v[12:13], v[8:9], v[96:97], v[12:13] op_sel_hi:[0,1,1]
	v_pk_fma_f32 v[10:11], v[8:9], v[106:107], v[10:11] op_sel_hi:[0,1,1]
	v_pk_fma_f32 v[96:97], v[8:9], v[108:109], v[102:103] op_sel_hi:[0,1,1]
	v_pk_fma_f32 v[100:101], v[8:9], v[148:149], v[100:101] op_sel_hi:[0,1,1]
	v_cvt_pk_f32_fp8_e32 v[102:103], v161
	v_cvt_pk_f32_fp8_sdwa v[106:107], v161 src0_sel:WORD_1
	v_cvt_pk_f32_fp8_e32 v[108:109], v160
	v_cvt_pk_f32_fp8_sdwa v[148:149], v160 src0_sel:WORD_1
	v_pk_fma_f32 v[102:103], v[8:9], v[102:103], v[104:105] op_sel_hi:[0,1,1]
	v_pk_fma_f32 v[104:105], v[8:9], v[106:107], v[98:99] op_sel_hi:[0,1,1]
	v_pk_fma_f32 v[6:7], v[8:9], v[108:109], v[6:7] op_sel_hi:[0,1,1]
	v_pk_fma_f32 v[106:107], v[8:9], v[148:149], v[94:95] op_sel_hi:[0,1,1]
	v_cvt_pk_f32_fp8_sdwa v[94:95], v159 src0_sel:WORD_1
	v_cvt_pk_f32_fp8_e32 v[98:99], v159
	v_cvt_pk_f32_fp8_sdwa v[108:109], v158 src0_sel:WORD_1
	v_cvt_pk_f32_fp8_e32 v[148:149], v158
	v_pk_fma_f32 v[152:153], v[8:9], v[94:95], v[10:11] op_sel:[1,0,0]
	v_pk_fma_f32 v[154:155], v[8:9], v[98:99], v[12:13] op_sel:[1,0,0]
	v_pk_fma_f32 v[98:99], v[8:9], v[108:109], v[100:101] op_sel:[1,0,0]
	v_pk_fma_f32 v[100:101], v[8:9], v[148:149], v[96:97] op_sel:[1,0,0]
	v_cvt_pk_f32_fp8_sdwa v[10:11], v157 src0_sel:WORD_1
	v_cvt_pk_f32_fp8_e32 v[12:13], v157
	v_cvt_pk_f32_fp8_sdwa v[108:109], v156 src0_sel:WORD_1
	v_cvt_pk_f32_fp8_e32 v[148:149], v156
	v_pk_fma_f32 v[94:95], v[8:9], v[10:11], v[104:105] op_sel:[1,0,0]
	v_pk_fma_f32 v[96:97], v[8:9], v[12:13], v[102:103] op_sel:[1,0,0]
	v_pk_fma_f32 v[10:11], v[8:9], v[108:109], v[106:107] op_sel:[1,0,0]
	v_pk_fma_f32 v[12:13], v[8:9], v[148:149], v[6:7] op_sel:[1,0,0]
	v_pk_mov_b32 v[6:7], v[154:155], v[152:153] op_sel:[1,0]
	v_mov_b32_e32 v8, v154
	v_mov_b32_e32 v9, v153
	v_pk_add_f32 v[6:7], v[6:7], v[8:9]
	v_pk_mov_b32 v[8:9], v[100:101], v[98:99] op_sel:[1,0]
	v_mov_b32_e32 v102, v100
	v_mov_b32_e32 v103, v99
	v_pk_add_f32 v[8:9], v[8:9], v[102:103]
	v_add_f32_e32 v6, v6, v7
	v_pk_add_f32 v[8:9], v[8:9], v[8:9] op_sel:[0,1] op_sel_hi:[1,0]
	v_add_f32_e32 v6, 0, v6
	v_add_f32_e32 v102, v96, v97
	v_add_f32_e32 v104, v94, v95
	v_mov_b32_e32 v7, v12
	v_mov_b32_e32 v9, v13
	v_mov_b32_e32 v103, v10
	v_mov_b32_e32 v105, v11
	v_pk_add_f32 v[6:7], v[6:7], v[8:9]
	v_pk_add_f32 v[8:9], v[102:103], v[104:105]
	s_lshl_b64 s[6:7], s[24:25], 12
	v_pk_add_f32 v[6:7], v[6:7], v[8:9]
	s_add_u32 s26, s8, s6
	v_add_f32_e32 v6, v6, v7
	ds_bpermute_b32 v7, v126, v6
	s_addc_u32 s27, s9, s7
	s_waitcnt lgkmcnt(0)
	v_add_f32_e32 v6, v6, v7
	ds_bpermute_b32 v7, v127, v6
	s_waitcnt lgkmcnt(0)
	v_add_f32_e32 v6, v6, v7
	ds_bpermute_b32 v7, v128, v6
	s_waitcnt lgkmcnt(0)
	v_add_f32_e32 v6, v6, v7
	ds_bpermute_b32 v7, v129, v6
	s_waitcnt lgkmcnt(0)
	v_add_f32_e32 v6, v6, v7
	ds_bpermute_b32 v7, v130, v6
	s_waitcnt lgkmcnt(0)
	v_add_f32_e32 v6, v6, v7
	ds_bpermute_b32 v7, v131, v6
	s_waitcnt lgkmcnt(0)
	v_add_f32_e32 v106, v6, v7
	v_fmamk_f32 v155, v106, 0xba800000, v155
	v_fmac_f32_e32 v154, 0xba800000, v106
	v_fmamk_f32 v153, v106, 0xba800000, v153
	v_fmac_f32_e32 v152, 0xba800000, v106
	v_pk_mul_f32 v[6:7], v[152:153], v[152:153]
	v_pk_mul_f32 v[8:9], v[154:155], v[154:155]
	v_fmamk_f32 v99, v106, 0xba800000, v99
	v_pk_mov_b32 v[102:103], v[8:9], v[6:7] op_sel:[1,0]
	v_mov_b32_e32 v9, v7
	v_pk_add_f32 v[6:7], v[102:103], v[8:9]
	v_fmac_f32_e32 v98, 0xba800000, v106
	v_fmamk_f32 v101, v106, 0xba800000, v101
	v_fmac_f32_e32 v100, 0xba800000, v106
	v_pk_add_f32 v[6:7], v[6:7], v[6:7] op_sel_hi:[0,1]
	v_pk_mul_f32 v[8:9], v[98:99], v[98:99]
	v_pk_mul_f32 v[102:103], v[100:101], v[100:101]
	v_fmac_f32_e32 v96, 0xba800000, v106
	v_pk_mov_b32 v[104:105], v[102:103], v[8:9] op_sel:[1,0]
	v_mov_b32_e32 v103, v9
	v_fmac_f32_e32 v94, 0xba800000, v106
	v_fmamk_f32 v97, v106, 0xba800000, v97
	v_mul_f32_e32 v6, v96, v96
	v_pk_add_f32 v[8:9], v[104:105], v[102:103]
	v_fmamk_f32 v95, v106, 0xba800000, v95
	v_pk_fma_f32 v[102:103], v[96:97], v[96:97], v[6:7] op_sel_hi:[1,1,0]
	v_mul_f32_e32 v6, v94, v94
	v_pk_add_f32 v[8:9], v[8:9], v[8:9] op_sel_hi:[0,1]
	v_pk_fma_f32 v[104:105], v[94:95], v[94:95], v[6:7] op_sel_hi:[1,1,0]
	v_fmamk_f32 v11, v106, 0xba800000, v11
	v_fmac_f32_e32 v10, 0xba800000, v106
	v_fmamk_f32 v13, v106, 0xba800000, v13
	v_fmac_f32_e32 v12, 0xba800000, v106
	v_mul_f32_e32 v102, v12, v12
	v_mul_f32_e32 v104, v13, v13
	v_mul_f32_e32 v6, v10, v10
	v_mul_f32_e32 v8, v11, v11
	v_pk_add_f32 v[102:103], v[102:103], v[104:105]
	v_pk_add_f32 v[6:7], v[6:7], v[8:9]
	s_nop 0
	v_pk_add_f32 v[6:7], v[102:103], v[6:7]
	s_nop 0
	v_add_f32_e32 v102, v6, v7
	ds_bpermute_b32 v103, v126, v102
	s_waitcnt lgkmcnt(0)
	v_add_f32_e32 v102, v102, v103
	ds_bpermute_b32 v103, v127, v102
	s_waitcnt lgkmcnt(0)
	v_add_f32_e32 v102, v102, v103
	ds_bpermute_b32 v103, v128, v102
	s_waitcnt lgkmcnt(0)
	v_add_f32_e32 v102, v102, v103
	ds_bpermute_b32 v103, v129, v102
	s_waitcnt lgkmcnt(0)
	v_add_f32_e32 v102, v102, v103
	ds_bpermute_b32 v103, v130, v102
	s_waitcnt lgkmcnt(0)
	v_add_f32_e32 v102, v102, v103
	ds_bpermute_b32 v103, v131, v102
	s_waitcnt lgkmcnt(0)
	v_add_f32_e32 v102, v102, v103
	v_fmamk_f32 v102, v102, 0x3a800000, v240
	v_mul_f32_e32 v103, 0x4f800000, v102
	v_cmp_gt_f32_e32 vcc, s36, v102
	s_nop 1
	v_cndmask_b32_e32 v102, v102, v103, vcc
	v_sqrt_f32_e32 v103, v102
	s_nop 0
	v_add_u32_e32 v104, -1, v103
	v_fma_f32 v105, -v104, v103, v102
	v_cmp_ge_f32_e64 s[6:7], 0, v105
	v_add_u32_e32 v105, 1, v103
	s_nop 0
	v_cndmask_b32_e64 v104, v103, v104, s[6:7]
	v_fma_f32 v103, -v105, v103, v102
	v_cmp_lt_f32_e64 s[6:7], 0, v103
	s_nop 1
	v_cndmask_b32_e64 v103, v104, v105, s[6:7]
	v_mul_f32_e32 v104, 0x37800000, v103
	v_cndmask_b32_e32 v103, v103, v104, vcc
	v_cmp_class_f32_e32 vcc, v102, v234
	s_and_b64 s[6:7], s[14:15], exec
	s_nop 0
	v_cndmask_b32_e32 v102, v103, v102, vcc
	v_div_scale_f32 v103, s[6:7], v102, v102, 1.0
	v_rcp_f32_e32 v104, v103
	s_cselect_b32 s7, s27, 0
	s_cselect_b32 s6, s26, 0
	s_cmp_lg_u64 s[6:7], 0
	v_fma_f32 v105, -v103, v104, 1.0
	v_fmac_f32_e32 v104, v105, v104
	v_div_scale_f32 v105, vcc, 1.0, v102, 1.0
	v_mul_f32_e32 v106, v105, v104
	v_fma_f32 v107, -v103, v106, v105
	v_fmac_f32_e32 v106, v107, v104
	v_fma_f32 v103, -v103, v106, v105
	v_div_fmas_f32 v103, v103, v104, v106
	v_div_fixup_f32 v106, v103, v102, 1.0
	v_pk_mul_f32 v[102:103], v[154:155], v[106:107] op_sel_hi:[1,0]
	v_pk_mul_f32 v[108:109], v[152:153], v[106:107] op_sel_hi:[1,0]
	s_cselect_b64 s[26:27], -1, 0
	s_cmp_eq_u64 s[6:7], 0
	v_lshl_add_u64 v[104:105], v[30:31], 2, s[6:7]
	v_pk_fma_f32 v[8:9], v[176:177], v[108:109], v[194:195]
	v_pk_fma_f32 v[6:7], v[174:175], v[102:103], v[192:193]
	s_cbranch_scc1 .LBB0_1266
	global_store_dwordx4 v[104:105], v[6:9], off
